# router first sweep: next iteration's x/delta/gain/scale loads issued into shadow VGPRs before the current iteration's compute (software pipelining)
# speedup vs baseline: 1.0242x; 1.0005x over previous
.LBB0_1028:
	s_ashr_i32 s35, s34, 31
	s_lshl_b64 s[18:19], s[34:35], 12
	s_lshl_b64 s[14:15], s[34:35], 13
	v_lshl_add_u64 v[84:85], v[38:39], 0, s[18:19]
	v_lshl_add_u64 v[86:87], v[42:43], 0, s[14:15]
	s_mov_b32 s16, 0
	v_mov_b32_e32 v88, v32
	v_mov_b32_e32 v80, 0
	v_mov_b32_e32 v81, v33
	v_mov_b32_e32 v82, 0
	v_mov_b32_e32 v83, v33
	v_mov_b32_e32 v60, 0
	v_mov_b32_e32 v61, v33
	v_mov_b32_e32 v56, 0
	v_mov_b32_e32 v57, v33
	v_mov_b32_e32 v54, 0
	v_mov_b32_e32 v55, v33
	v_mov_b32_e32 v50, 0
	v_mov_b32_e32 v51, v33
	v_mov_b32_e32 v46, 0
	v_mov_b32_e32 v47, v33
	v_mov_b32_e32 v30, 0
	v_mov_b32_e32 v31, v33
	v_mov_b32_e32 v28, 0
	v_mov_b32_e32 v29, v33
	v_mov_b32_e32 v24, 0
	v_mov_b32_e32 v25, v33
	v_mov_b32_e32 v22, 0
	v_mov_b32_e32 v23, v33
	v_mov_b32_e32 v18, 0
	v_mov_b32_e32 v19, v33
	v_mov_b32_e32 v14, 0
	v_mov_b32_e32 v15, v33
	v_mov_b32_e32 v12, 0
	v_mov_b32_e32 v13, v33
	v_mov_b32_e32 v8, 0
	v_mov_b32_e32 v9, v33
	v_mov_b32_e32 v4, 0
	v_mov_b32_e32 v5, v33
	v_mov_b32_e32 v68, 0
	v_mov_b32_e32 v69, v33
	v_mov_b32_e32 v72, 0
	v_mov_b32_e32 v73, v33
	v_mov_b32_e32 v6, 0
	v_mov_b32_e32 v7, v33
	v_mov_b32_e32 v10, 0
	v_mov_b32_e32 v11, v33
	v_mov_b32_e32 v16, 0
	v_mov_b32_e32 v17, v33
	v_mov_b32_e32 v20, 0
	v_mov_b32_e32 v21, v33
	v_mov_b32_e32 v26, 0
	v_mov_b32_e32 v27, v33
	v_mov_b32_e32 v44, 0
	v_mov_b32_e32 v45, v33
	v_mov_b32_e32 v48, 0
	v_mov_b32_e32 v49, v33
	v_mov_b32_e32 v52, 0
	v_mov_b32_e32 v53, v33
	v_mov_b32_e32 v58, 0
	v_mov_b32_e32 v59, v33
	v_mov_b32_e32 v62, 0
	v_mov_b32_e32 v63, v33
	v_mov_b32_e32 v64, 0
	v_mov_b32_e32 v65, v33
	v_mov_b32_e32 v66, 0
	v_mov_b32_e32 v67, v33
	v_mov_b32_e32 v70, 0
	v_mov_b32_e32 v71, v33
	v_mov_b32_e32 v74, 0
	v_mov_b32_e32 v75, v33
	v_mov_b32_e32 v76, 0
	v_mov_b32_e32 v77, v33
	v_mov_b32_e32 v78, 0
	v_mov_b32_e32 v79, v33
	global_load_dwordx4 v[208:211], v[86:87], off
	global_load_dwordx2 v[212:213], v[84:85], off offset:-4096
	global_load_dwordx2 v[214:215], v[84:85], off
	v_add_co_u32_e32 v216, vcc, s5, v86
	s_nop 1
	v_addc_co_u32_e32 v217, vcc, -1, v87, vcc
	global_load_dwordx4 v[216:219], v[216:217], off
	v_add_co_u32_e32 v220, vcc, s6, v86
	s_nop 1
	v_addc_co_u32_e32 v221, vcc, -1, v87, vcc
	global_load_dwordx4 v[220:223], v[220:221], off
	v_add_co_u32_e32 v240, vcc, s7, v84
	s_nop 1
	v_addc_co_u32_e32 v241, vcc, -1, v85, vcc
	global_load_dwordx2 v[224:225], v[240:241], off offset:-4096
	global_load_dwordx2 v[226:227], v[240:241], off
	v_add_co_u32_e32 v228, vcc, s7, v86
	s_nop 1
	v_addc_co_u32_e32 v229, vcc, -1, v87, vcc
	global_load_dwordx4 v[228:231], v[228:229], off
	v_ashrrev_i32_e32 v89, 31, v88
	v_lshlrev_b64 v[242:243], 4, v[88:89]
	v_lshl_add_u64 v[232:233], s[28:29], 0, v[242:243]
	global_load_dwordx4 v[232:235], v[232:233], off
	v_ashrrev_i32_e32 v89, 31, v88
	v_lshlrev_b64 v[242:243], 4, v[88:89]
	v_lshl_add_u64 v[236:237], s[26:27], 0, v[242:243]
	global_load_dwordx4 v[236:239], v[236:237], off
.LBB0_1029:
	s_nop 0
	v_add_u32_e32 v111, s16, v108
	s_nop 0
	v_add_u32_e32 v145, s16, v107
	s_nop 0
	s_nop 0
	s_nop 0
	v_add_u32_e32 v156, s16, v106
	v_add_u32_e32 v157, s16, v105
	v_add_u32_e32 v89, 0x10000, v111
	v_add_u32_e32 v158, 0x10000, v145
	v_add_u32_e32 v162, 0x10000, v156
	v_add_u32_e32 v166, 0x10000, v157
	v_add_u32_e32 v178, 0x18000, v156
	v_add_u32_e32 v182, 0x18000, v157
	ds_read_b128 v[120:123], v111
	ds_read_b128 v[124:127], v111 offset:32768
	ds_read_b128 v[128:131], v145
	ds_read_b128 v[132:135], v145 offset:32768
	ds_read_b128 v[136:139], v156
	ds_read_b128 v[140:143], v156 offset:32768
	ds_read_b128 v[146:149], v157
	ds_read_b128 v[150:153], v157 offset:32768
	v_add_u32_e32 v111, 0x18000, v111
	v_add_u32_e32 v145, 0x18000, v145
	ds_read_b128 v[154:157], v89
	ds_read_b128 v[158:161], v158
	ds_read_b128 v[162:165], v162
	ds_read_b128 v[166:169], v166
	ds_read_b128 v[170:173], v111
	ds_read_b128 v[174:177], v145
	ds_read_b128 v[178:181], v178
	ds_read_b128 v[182:185], v182
	s_nop 0
	s_addk_i32 s16, 0x1000
	v_lshl_add_u64 v[84:85], v[84:85], 0, s[42:43]
	v_lshl_add_u64 v[86:87], v[86:87], 0, s[44:45]
	v_add_u32_e32 v88, 64, v88
	s_cmpk_eq_u32 s16, 0x8000
	s_waitcnt vmcnt(0)
	v_mov_b64_e32 v[0:1], v[208:209]
	v_mov_b64_e32 v[2:3], v[210:211]
	v_mov_b64_e32 v[96:97], v[212:213]
	v_mov_b64_e32 v[98:99], v[214:215]
	v_mov_b64_e32 v[112:113], v[216:217]
	v_mov_b64_e32 v[114:115], v[218:219]
	v_mov_b64_e32 v[116:117], v[220:221]
	v_mov_b64_e32 v[118:119], v[222:223]
	v_mov_b64_e32 v[94:95], v[224:225]
	v_mov_b64_e32 v[194:195], v[226:227]
	v_mov_b64_e32 v[90:91], v[228:229]
	v_mov_b64_e32 v[92:93], v[230:231]
	v_mov_b64_e32 v[186:187], v[232:233]
	v_mov_b64_e32 v[188:189], v[234:235]
	v_mov_b64_e32 v[190:191], v[236:237]
	v_mov_b64_e32 v[192:193], v[238:239]
	s_cbranch_scc1 .Lswp_skip_0
	global_load_dwordx4 v[208:211], v[86:87], off
	global_load_dwordx2 v[212:213], v[84:85], off offset:-4096
	global_load_dwordx2 v[214:215], v[84:85], off
	v_add_co_u32_e32 v216, vcc, s5, v86
	s_nop 1
	v_addc_co_u32_e32 v217, vcc, -1, v87, vcc
	global_load_dwordx4 v[216:219], v[216:217], off
	v_add_co_u32_e32 v220, vcc, s6, v86
	s_nop 1
	v_addc_co_u32_e32 v221, vcc, -1, v87, vcc
	global_load_dwordx4 v[220:223], v[220:221], off
	v_add_co_u32_e32 v240, vcc, s7, v84
	s_nop 1
	v_addc_co_u32_e32 v241, vcc, -1, v85, vcc
	global_load_dwordx2 v[224:225], v[240:241], off offset:-4096
	global_load_dwordx2 v[226:227], v[240:241], off
	v_add_co_u32_e32 v228, vcc, s7, v86
	s_nop 1
	v_addc_co_u32_e32 v229, vcc, -1, v87, vcc
	global_load_dwordx4 v[228:231], v[228:229], off
	v_ashrrev_i32_e32 v89, 31, v88
	v_lshlrev_b64 v[242:243], 4, v[88:89]
	v_lshl_add_u64 v[232:233], s[28:29], 0, v[242:243]
	global_load_dwordx4 v[232:235], v[232:233], off
	v_ashrrev_i32_e32 v89, 31, v88
	v_lshlrev_b64 v[242:243], 4, v[88:89]
	v_lshl_add_u64 v[236:237], s[26:27], 0, v[242:243]
	global_load_dwordx4 v[236:239], v[236:237], off
.Lswp_skip_0:
	v_mov_b32_e32 v196, v0
	v_lshlrev_b32_e32 v101, 16, v96
	v_lshlrev_b32_e32 v100, 16, v98
	v_and_b32_e32 v199, 0xffff0000, v96
	v_and_b32_e32 v198, 0xffff0000, v98
	v_lshlrev_b32_e32 v201, 16, v97
	v_lshlrev_b32_e32 v200, 16, v99
	v_and_b32_e32 v97, 0xffff0000, v97
	v_and_b32_e32 v96, 0xffff0000, v99
	v_mov_b32_e32 v0, v2
	v_mov_b32_e32 v203, v112
	v_mov_b32_e32 v202, v116
	v_lshlrev_b32_e32 v99, 16, v94
	v_lshlrev_b32_e32 v98, 16, v194
	v_and_b32_e32 v205, 0xffff0000, v94
	v_and_b32_e32 v204, 0xffff0000, v194
	v_mov_b32_e32 v112, v117
	v_lshlrev_b32_e32 v117, 16, v95
	v_mov_b32_e32 v207, v114
	v_and_b32_e32 v95, 0xffff0000, v95
	v_and_b32_e32 v94, 0xffff0000, v195
	v_mov_b32_e32 v114, v119
	v_mov_b32_e32 v197, v90
	v_mov_b32_e32 v90, v1
	v_mov_b32_e32 v1, v92
	v_mov_b32_e32 v92, v3
	v_lshlrev_b32_e32 v116, 16, v195
	v_mov_b32_e32 v206, v118
	v_pk_add_f32 v[2:3], v[202:203], v[98:99]
	v_pk_add_f32 v[98:99], v[112:113], v[204:205]
	v_pk_add_f32 v[94:95], v[114:115], v[94:95]
	v_pk_add_f32 v[90:91], v[90:91], v[198:199]
	v_pk_add_f32 v[92:93], v[92:93], v[96:97]
	v_pk_add_f32 v[112:113], v[206:207], v[116:117]
	v_pk_add_f32 v[100:101], v[196:197], v[100:101]
	v_pk_add_f32 v[0:1], v[0:1], v[200:201]
	v_pk_mul_f32 v[96:97], v[98:99], v[98:99]
	v_pk_mul_f32 v[114:115], v[94:95], v[94:95]
	v_pk_mul_f32 v[116:117], v[90:91], v[90:91]
	v_pk_mul_f32 v[118:119], v[92:93], v[92:93]
	v_add_f32_e32 v89, 1.0, v186
	v_add_f32_e32 v111, 1.0, v187
	v_pk_fma_f32 v[96:97], v[2:3], v[2:3], v[96:97]
	v_pk_fma_f32 v[114:115], v[112:113], v[112:113], v[114:115]
	v_pk_fma_f32 v[116:117], v[100:101], v[100:101], v[116:117]
	v_pk_fma_f32 v[118:119], v[0:1], v[0:1], v[118:119]
	v_mul_f32_e32 v89, v190, v89
	v_add_f32_e32 v145, 1.0, v188
	v_add_f32_e32 v186, 1.0, v189
	v_mul_f32_e32 v111, v191, v111
	v_pk_add_f32 v[96:97], v[96:97], v[114:115]
	v_pk_add_f32 v[114:115], v[116:117], v[118:119]
	v_mul_f32_e32 v116, v89, v3
	v_mul_f32_e32 v2, v89, v2
	v_mul_f32_e32 v118, v89, v101
	v_mul_f32_e32 v100, v89, v100
	v_mul_f32_e32 v145, v192, v145
	v_mul_f32_e32 v187, v193, v186
	v_mul_f32_e32 v186, v111, v99
	v_mul_f32_e32 v98, v111, v98
	v_mul_f32_e32 v188, v111, v91
	v_mul_f32_e32 v90, v111, v90
	s_waitcnt lgkmcnt(14)
	v_pk_fma_f32 v[78:79], v[116:117], v[120:121], v[78:79] op_sel_hi:[0,1,1]
	v_pk_fma_f32 v[76:77], v[116:117], v[122:123], v[76:77] op_sel_hi:[0,1,1]
	v_pk_fma_f32 v[52:53], v[2:3], v[120:121], v[52:53] op_sel_hi:[0,1,1]
	v_pk_fma_f32 v[48:49], v[2:3], v[122:123], v[48:49] op_sel_hi:[0,1,1]
	v_pk_fma_f32 v[72:73], v[120:121], v[118:119], v[72:73] op_sel_hi:[1,0,1]
	v_pk_fma_f32 v[68:69], v[122:123], v[118:119], v[68:69] op_sel_hi:[1,0,1]
	v_pk_fma_f32 v[28:29], v[120:121], v[100:101], v[28:29] op_sel_hi:[1,0,1]
	v_pk_fma_f32 v[24:25], v[122:123], v[100:101], v[24:25] op_sel_hi:[1,0,1]
	s_waitcnt lgkmcnt(13)
	v_pk_fma_f32 v[74:75], v[116:117], v[128:129], v[74:75] op_sel_hi:[0,1,1]
	v_pk_fma_f32 v[70:71], v[116:117], v[130:131], v[70:71] op_sel_hi:[0,1,1]
	v_pk_fma_f32 v[44:45], v[2:3], v[128:129], v[44:45] op_sel_hi:[0,1,1]
	v_pk_fma_f32 v[26:27], v[2:3], v[130:131], v[26:27] op_sel_hi:[0,1,1]
	v_pk_fma_f32 v[60:61], v[128:129], v[118:119], v[60:61] op_sel_hi:[1,0,1]
	v_pk_fma_f32 v[56:57], v[130:131], v[118:119], v[56:57] op_sel_hi:[1,0,1]
	v_pk_fma_f32 v[22:23], v[128:129], v[100:101], v[22:23] op_sel_hi:[1,0,1]
	v_pk_fma_f32 v[18:19], v[130:131], v[100:101], v[18:19] op_sel_hi:[1,0,1]
	s_waitcnt lgkmcnt(11)
	v_pk_fma_f32 v[66:67], v[116:117], v[136:137], v[66:67] op_sel_hi:[0,1,1]
	v_pk_fma_f32 v[64:65], v[116:117], v[138:139], v[64:65] op_sel_hi:[0,1,1]
	v_pk_fma_f32 v[20:21], v[2:3], v[136:137], v[20:21] op_sel_hi:[0,1,1]
	v_pk_fma_f32 v[16:17], v[2:3], v[138:139], v[16:17] op_sel_hi:[0,1,1]
	v_pk_fma_f32 v[54:55], v[118:119], v[136:137], v[54:55] op_sel_hi:[0,1,1]
	v_pk_fma_f32 v[50:51], v[118:119], v[138:139], v[50:51] op_sel_hi:[0,1,1]
	v_pk_fma_f32 v[14:15], v[136:137], v[100:101], v[14:15] op_sel_hi:[1,0,1]
	v_pk_fma_f32 v[12:13], v[138:139], v[100:101], v[12:13] op_sel_hi:[1,0,1]
	s_waitcnt lgkmcnt(9)
	v_pk_fma_f32 v[62:63], v[116:117], v[146:147], v[62:63] op_sel_hi:[0,1,1]
	v_pk_fma_f32 v[58:59], v[116:117], v[148:149], v[58:59] op_sel_hi:[0,1,1]
	v_pk_fma_f32 v[10:11], v[2:3], v[146:147], v[10:11] op_sel_hi:[0,1,1]
	v_pk_fma_f32 v[2:3], v[2:3], v[148:149], v[6:7] op_sel_hi:[0,1,1]
	v_pk_fma_f32 v[6:7], v[118:119], v[146:147], v[46:47] op_sel_hi:[0,1,1]
	v_pk_fma_f32 v[30:31], v[118:119], v[148:149], v[30:31] op_sel_hi:[0,1,1]
	v_pk_fma_f32 v[8:9], v[146:147], v[100:101], v[8:9] op_sel_hi:[1,0,1]
	v_pk_fma_f32 v[4:5], v[148:149], v[100:101], v[4:5] op_sel_hi:[1,0,1]
	v_mul_f32_e32 v190, v145, v113
	v_mul_f32_e32 v112, v145, v112
	v_mul_f32_e32 v192, v145, v1
	v_mul_f32_e32 v0, v145, v0
	v_pk_fma_f32 v[46:47], v[186:187], v[124:125], v[78:79] op_sel_hi:[0,1,1]
	v_pk_fma_f32 v[76:77], v[186:187], v[126:127], v[76:77] op_sel_hi:[0,1,1]
	v_pk_fma_f32 v[52:53], v[98:99], v[124:125], v[52:53] op_sel_hi:[0,1,1]
	v_pk_fma_f32 v[48:49], v[98:99], v[126:127], v[48:49] op_sel_hi:[0,1,1]
	v_pk_fma_f32 v[72:73], v[188:189], v[124:125], v[72:73] op_sel_hi:[0,1,1]
	v_pk_fma_f32 v[68:69], v[188:189], v[126:127], v[68:69] op_sel_hi:[0,1,1]
	v_pk_fma_f32 v[28:29], v[90:91], v[124:125], v[28:29] op_sel_hi:[0,1,1]
	v_pk_fma_f32 v[24:25], v[90:91], v[126:127], v[24:25] op_sel_hi:[0,1,1]
	v_pk_fma_f32 v[74:75], v[186:187], v[132:133], v[74:75] op_sel_hi:[0,1,1]
	v_pk_fma_f32 v[70:71], v[186:187], v[134:135], v[70:71] op_sel_hi:[0,1,1]
	v_pk_fma_f32 v[44:45], v[98:99], v[132:133], v[44:45] op_sel_hi:[0,1,1]
	v_pk_fma_f32 v[26:27], v[98:99], v[134:135], v[26:27] op_sel_hi:[0,1,1]
	v_pk_fma_f32 v[60:61], v[188:189], v[132:133], v[60:61] op_sel_hi:[0,1,1]
	v_pk_fma_f32 v[56:57], v[188:189], v[134:135], v[56:57] op_sel_hi:[0,1,1]
	v_pk_fma_f32 v[22:23], v[90:91], v[132:133], v[22:23] op_sel_hi:[0,1,1]
	v_pk_fma_f32 v[18:19], v[90:91], v[134:135], v[18:19] op_sel_hi:[0,1,1]
	v_pk_fma_f32 v[66:67], v[186:187], v[140:141], v[66:67] op_sel_hi:[0,1,1]
	v_pk_fma_f32 v[64:65], v[186:187], v[142:143], v[64:65] op_sel_hi:[0,1,1]
	v_pk_fma_f32 v[20:21], v[98:99], v[140:141], v[20:21] op_sel_hi:[0,1,1]
	v_pk_fma_f32 v[16:17], v[98:99], v[142:143], v[16:17] op_sel_hi:[0,1,1]
	v_pk_fma_f32 v[54:55], v[188:189], v[140:141], v[54:55] op_sel_hi:[0,1,1]
	v_pk_fma_f32 v[50:51], v[188:189], v[142:143], v[50:51] op_sel_hi:[0,1,1]
	v_pk_fma_f32 v[14:15], v[90:91], v[140:141], v[14:15] op_sel_hi:[0,1,1]
	v_pk_fma_f32 v[12:13], v[90:91], v[142:143], v[12:13] op_sel_hi:[0,1,1]
	s_waitcnt lgkmcnt(8)
	v_pk_fma_f32 v[62:63], v[186:187], v[150:151], v[62:63] op_sel_hi:[0,1,1]
	v_pk_fma_f32 v[58:59], v[186:187], v[152:153], v[58:59] op_sel_hi:[0,1,1]
	v_pk_fma_f32 v[10:11], v[98:99], v[150:151], v[10:11] op_sel_hi:[0,1,1]
	v_pk_fma_f32 v[2:3], v[98:99], v[152:153], v[2:3] op_sel_hi:[0,1,1]
	v_pk_fma_f32 v[6:7], v[188:189], v[150:151], v[6:7] op_sel_hi:[0,1,1]
	v_pk_fma_f32 v[30:31], v[188:189], v[152:153], v[30:31] op_sel_hi:[0,1,1]
	v_pk_fma_f32 v[8:9], v[90:91], v[150:151], v[8:9] op_sel_hi:[0,1,1]
	v_pk_fma_f32 v[4:5], v[90:91], v[152:153], v[4:5] op_sel_hi:[0,1,1]
	v_mul_f32_e32 v194, v187, v95
	v_mul_f32_e32 v94, v187, v94
	v_mul_f32_e32 v196, v187, v93
	v_mul_f32_e32 v92, v187, v92
	s_waitcnt lgkmcnt(7)
	v_pk_fma_f32 v[46:47], v[190:191], v[154:155], v[46:47] op_sel_hi:[0,1,1]
	v_pk_fma_f32 v[76:77], v[190:191], v[156:157], v[76:77] op_sel_hi:[0,1,1]
	v_pk_fma_f32 v[52:53], v[112:113], v[154:155], v[52:53] op_sel_hi:[0,1,1]
	v_pk_fma_f32 v[48:49], v[112:113], v[156:157], v[48:49] op_sel_hi:[0,1,1]
	v_pk_fma_f32 v[72:73], v[192:193], v[154:155], v[72:73] op_sel_hi:[0,1,1]
	v_pk_fma_f32 v[68:69], v[192:193], v[156:157], v[68:69] op_sel_hi:[0,1,1]
	v_pk_fma_f32 v[28:29], v[0:1], v[154:155], v[28:29] op_sel_hi:[0,1,1]
	v_pk_fma_f32 v[24:25], v[0:1], v[156:157], v[24:25] op_sel_hi:[0,1,1]
	s_waitcnt lgkmcnt(6)
	v_pk_fma_f32 v[74:75], v[190:191], v[158:159], v[74:75] op_sel_hi:[0,1,1]
	v_pk_fma_f32 v[70:71], v[190:191], v[160:161], v[70:71] op_sel_hi:[0,1,1]
	v_pk_fma_f32 v[44:45], v[112:113], v[158:159], v[44:45] op_sel_hi:[0,1,1]
	v_pk_fma_f32 v[26:27], v[112:113], v[160:161], v[26:27] op_sel_hi:[0,1,1]
	v_pk_fma_f32 v[60:61], v[192:193], v[158:159], v[60:61] op_sel_hi:[0,1,1]
	v_pk_fma_f32 v[56:57], v[192:193], v[160:161], v[56:57] op_sel_hi:[0,1,1]
	v_pk_fma_f32 v[22:23], v[0:1], v[158:159], v[22:23] op_sel_hi:[0,1,1]
	v_pk_fma_f32 v[18:19], v[0:1], v[160:161], v[18:19] op_sel_hi:[0,1,1]
	s_waitcnt lgkmcnt(5)
	v_pk_fma_f32 v[66:67], v[190:191], v[162:163], v[66:67] op_sel_hi:[0,1,1]
	v_pk_fma_f32 v[64:65], v[190:191], v[164:165], v[64:65] op_sel_hi:[0,1,1]
	v_pk_fma_f32 v[20:21], v[112:113], v[162:163], v[20:21] op_sel_hi:[0,1,1]
	v_pk_fma_f32 v[16:17], v[112:113], v[164:165], v[16:17] op_sel_hi:[0,1,1]
	v_pk_fma_f32 v[54:55], v[192:193], v[162:163], v[54:55] op_sel_hi:[0,1,1]
	v_pk_fma_f32 v[50:51], v[192:193], v[164:165], v[50:51] op_sel_hi:[0,1,1]
	v_pk_fma_f32 v[14:15], v[0:1], v[162:163], v[14:15] op_sel_hi:[0,1,1]
	v_pk_fma_f32 v[12:13], v[0:1], v[164:165], v[12:13] op_sel_hi:[0,1,1]
	s_waitcnt lgkmcnt(4)
	v_pk_fma_f32 v[62:63], v[190:191], v[166:167], v[62:63] op_sel_hi:[0,1,1]
	v_pk_fma_f32 v[58:59], v[190:191], v[168:169], v[58:59] op_sel_hi:[0,1,1]
	v_pk_fma_f32 v[10:11], v[112:113], v[166:167], v[10:11] op_sel_hi:[0,1,1]
	v_pk_fma_f32 v[2:3], v[112:113], v[168:169], v[2:3] op_sel_hi:[0,1,1]
	v_pk_fma_f32 v[90:91], v[192:193], v[166:167], v[6:7] op_sel_hi:[0,1,1]
	v_pk_fma_f32 v[30:31], v[192:193], v[168:169], v[30:31] op_sel_hi:[0,1,1]
	v_pk_fma_f32 v[8:9], v[0:1], v[166:167], v[8:9] op_sel_hi:[0,1,1]
	v_pk_fma_f32 v[0:1], v[0:1], v[168:169], v[4:5] op_sel_hi:[0,1,1]
	v_pk_add_f32 v[82:83], v[82:83], v[96:97]
	v_pk_add_f32 v[80:81], v[80:81], v[114:115]
	s_waitcnt lgkmcnt(3)
	v_pk_fma_f32 v[78:79], v[194:195], v[170:171], v[46:47] op_sel_hi:[0,1,1]
	v_pk_fma_f32 v[76:77], v[194:195], v[172:173], v[76:77] op_sel_hi:[0,1,1]
	v_pk_fma_f32 v[52:53], v[94:95], v[170:171], v[52:53] op_sel_hi:[0,1,1]
	v_pk_fma_f32 v[48:49], v[94:95], v[172:173], v[48:49] op_sel_hi:[0,1,1]
	v_pk_fma_f32 v[72:73], v[196:197], v[170:171], v[72:73] op_sel_hi:[0,1,1]
	v_pk_fma_f32 v[68:69], v[196:197], v[172:173], v[68:69] op_sel_hi:[0,1,1]
	v_pk_fma_f32 v[28:29], v[92:93], v[170:171], v[28:29] op_sel_hi:[0,1,1]
	v_pk_fma_f32 v[24:25], v[92:93], v[172:173], v[24:25] op_sel_hi:[0,1,1]
	s_waitcnt lgkmcnt(2)
	v_pk_fma_f32 v[74:75], v[194:195], v[174:175], v[74:75] op_sel_hi:[0,1,1]
	v_pk_fma_f32 v[70:71], v[194:195], v[176:177], v[70:71] op_sel_hi:[0,1,1]
	v_pk_fma_f32 v[44:45], v[94:95], v[174:175], v[44:45] op_sel_hi:[0,1,1]
	v_pk_fma_f32 v[26:27], v[94:95], v[176:177], v[26:27] op_sel_hi:[0,1,1]
	v_pk_fma_f32 v[60:61], v[196:197], v[174:175], v[60:61] op_sel_hi:[0,1,1]
	v_pk_fma_f32 v[56:57], v[196:197], v[176:177], v[56:57] op_sel_hi:[0,1,1]
	v_pk_fma_f32 v[22:23], v[92:93], v[174:175], v[22:23] op_sel_hi:[0,1,1]
	v_pk_fma_f32 v[18:19], v[92:93], v[176:177], v[18:19] op_sel_hi:[0,1,1]
	s_waitcnt lgkmcnt(1)
	v_pk_fma_f32 v[66:67], v[194:195], v[178:179], v[66:67] op_sel_hi:[0,1,1]
	v_pk_fma_f32 v[64:65], v[194:195], v[180:181], v[64:65] op_sel_hi:[0,1,1]
	v_pk_fma_f32 v[20:21], v[94:95], v[178:179], v[20:21] op_sel_hi:[0,1,1]
	v_pk_fma_f32 v[16:17], v[94:95], v[180:181], v[16:17] op_sel_hi:[0,1,1]
	v_pk_fma_f32 v[54:55], v[196:197], v[178:179], v[54:55] op_sel_hi:[0,1,1]
	v_pk_fma_f32 v[50:51], v[196:197], v[180:181], v[50:51] op_sel_hi:[0,1,1]
	v_pk_fma_f32 v[14:15], v[92:93], v[178:179], v[14:15] op_sel_hi:[0,1,1]
	v_pk_fma_f32 v[12:13], v[92:93], v[180:181], v[12:13] op_sel_hi:[0,1,1]
	s_waitcnt lgkmcnt(0)
	v_pk_fma_f32 v[62:63], v[194:195], v[182:183], v[62:63] op_sel_hi:[0,1,1]
	v_pk_fma_f32 v[58:59], v[194:195], v[184:185], v[58:59] op_sel_hi:[0,1,1]
	v_pk_fma_f32 v[10:11], v[94:95], v[182:183], v[10:11] op_sel_hi:[0,1,1]
	v_pk_fma_f32 v[6:7], v[94:95], v[184:185], v[2:3] op_sel_hi:[0,1,1]
	v_pk_fma_f32 v[46:47], v[196:197], v[182:183], v[90:91] op_sel_hi:[0,1,1]
	v_pk_fma_f32 v[30:31], v[196:197], v[184:185], v[30:31] op_sel_hi:[0,1,1]
	v_pk_fma_f32 v[8:9], v[92:93], v[182:183], v[8:9] op_sel_hi:[0,1,1]
	v_pk_fma_f32 v[4:5], v[92:93], v[184:185], v[0:1] op_sel_hi:[0,1,1]
	s_cbranch_scc0 .LBB0_1029
	v_mov_b32_e32 v0, v144
	s_add_u32 s20, s30, s14
	v_lshlrev_b32_e32 v86, 2, v0
	v_xor_b32_e32 v0, 4, v86
	ds_bpermute_b32 v1, v0, v83
	v_mov_b32_e32 v0, v144
	v_xor_b32_e32 v2, 8, v86
	v_lshlrev_b32_e32 v87, 2, v0
	v_xor_b32_e32 v0, 4, v87
	ds_bpermute_b32 v0, v0, v82
	v_xor_b32_e32 v84, 8, v87
	s_addc_u32 s21, s31, s15
	s_ashr_i32 s37, s36, 31
	s_ashr_i32 s39, s38, 31
	s_waitcnt lgkmcnt(0)
	v_pk_add_f32 v[0:1], v[82:83], v[0:1]
	ds_bpermute_b32 v3, v2, v1
	ds_bpermute_b32 v2, v84, v0
	v_xor_b32_e32 v82, 16, v86
	v_xor_b32_e32 v83, 16, v87
	s_ashr_i32 s41, s40, 31
	s_lshl_b64 s[50:51], s[36:37], 12
	s_waitcnt lgkmcnt(0)
	v_pk_add_f32 v[0:1], v[0:1], v[2:3]
	ds_bpermute_b32 v3, v82, v1
	ds_bpermute_b32 v2, v83, v0
	v_xor_b32_e32 v82, 32, v86
	v_xor_b32_e32 v83, 32, v87
	s_lshl_b64 s[52:53], s[38:39], 12
	s_lshl_b64 s[60:61], s[40:41], 12
	s_waitcnt lgkmcnt(0)
	v_pk_add_f32 v[0:1], v[0:1], v[2:3]
	ds_bpermute_b32 v3, v82, v1
	ds_bpermute_b32 v2, v83, v0
	v_xor_b32_e32 v82, 64, v86
	v_xor_b32_e32 v83, 64, v87
	v_lshl_add_u64 v[84:85], v[36:37], 0, s[18:19]
	s_waitcnt lgkmcnt(0)
	v_pk_add_f32 v[0:1], v[0:1], v[2:3]
	ds_bpermute_b32 v3, v82, v1
	ds_bpermute_b32 v2, v83, v0
	v_xor_b32_e32 v82, 0x80, v86
	v_xor_b32_e32 v83, 0x80, v87
	s_waitcnt lgkmcnt(0)
	v_pk_add_f32 v[0:1], v[0:1], v[2:3]
	ds_bpermute_b32 v3, v82, v1
	v_mov_b32_e32 v82, v144
	ds_bpermute_b32 v2, v83, v0
	v_lshlrev_b32_e32 v86, 2, v82
	v_xor_b32_e32 v82, 4, v86
	ds_bpermute_b32 v83, v82, v81
	v_mov_b32_e32 v82, v144
	v_xor_b32_e32 v88, 8, v86
	v_lshlrev_b32_e32 v87, 2, v82
	v_xor_b32_e32 v82, 4, v87
	ds_bpermute_b32 v82, v82, v80
	v_xor_b32_e32 v89, 8, v87
	v_xor_b32_e32 v90, 16, v87
	s_waitcnt lgkmcnt(2)
	v_pk_add_f32 v[0:1], v[0:1], v[2:3]
	v_mov_b64_e32 v[2:3], s[48:49]
	s_waitcnt lgkmcnt(0)
	v_pk_add_f32 v[80:81], v[80:81], v[82:83]
	ds_bpermute_b32 v83, v88, v81
	ds_bpermute_b32 v82, v89, v80
	v_xor_b32_e32 v89, 16, v86
	v_pk_fma_f32 v[0:1], v[0:1], s[46:47], v[2:3] op_sel_hi:[1,0,0]
	s_waitcnt lgkmcnt(0)
	v_pk_add_f32 v[80:81], v[80:81], v[82:83]
	ds_bpermute_b32 v83, v89, v81
	ds_bpermute_b32 v82, v90, v80
	v_mul_f32_e32 v88, 0x4b800000, v1
	v_cmp_gt_f32_e32 vcc, s8, v1
	v_xor_b32_e32 v89, 32, v87
	v_xor_b32_e32 v90, 64, v87
	v_cndmask_b32_e32 v1, v1, v88, vcc
	v_xor_b32_e32 v88, 32, v86
	s_waitcnt lgkmcnt(0)
	v_pk_add_f32 v[80:81], v[80:81], v[82:83]
	ds_bpermute_b32 v83, v88, v81
	ds_bpermute_b32 v82, v89, v80
	v_xor_b32_e32 v89, 64, v86
	v_mul_f32_e32 v88, 0x4b800000, v0
	v_cmp_gt_f32_e64 s[14:15], s8, v0
	v_rsq_f32_e32 v1, v1
	s_waitcnt lgkmcnt(0)
	v_pk_add_f32 v[80:81], v[80:81], v[82:83]
	ds_bpermute_b32 v83, v89, v81
	ds_bpermute_b32 v82, v90, v80
	v_cndmask_b32_e64 v0, v0, v88, s[14:15]
	v_rsq_f32_e32 v88, v0
	v_xor_b32_e32 v0, 0x80, v86
	v_xor_b32_e32 v86, 0x80, v87
	s_waitcnt lgkmcnt(0)
	v_pk_add_f32 v[80:81], v[80:81], v[82:83]
	ds_bpermute_b32 v83, v0, v81
	ds_bpermute_b32 v82, v86, v80
	v_mul_f32_e32 v0, 0x45800000, v1
	v_cndmask_b32_e32 v0, v1, v0, vcc
	v_mul_f32_e32 v1, 0x45800000, v88
	s_waitcnt lgkmcnt(0)
	v_pk_add_f32 v[80:81], v[80:81], v[82:83]
	s_nop 0
	v_pk_fma_f32 v[2:3], v[80:81], s[46:47], v[2:3] op_sel_hi:[1,0,0]
	s_nop 0
	v_mul_f32_e32 v80, 0x4b800000, v3
	v_cmp_gt_f32_e32 vcc, s8, v3
	v_cmp_gt_f32_e64 s[16:17], s8, v2
	s_nop 0
	v_cndmask_b32_e32 v3, v3, v80, vcc
	v_mul_f32_e32 v80, 0x4b800000, v2
	v_rsq_f32_e32 v3, v3
	v_cndmask_b32_e64 v2, v2, v80, s[16:17]
	v_rsq_f32_e32 v81, v2
	v_cndmask_b32_e64 v2, v88, v1, s[14:15]
	s_load_dwordx2 s[14:15], s[22:23], 0x118
	v_mul_f32_e32 v1, 0x45800000, v3
	v_cndmask_b32_e32 v80, v3, v1, vcc
	v_mul_f32_e32 v1, 0x45800000, v81
	v_cndmask_b32_e64 v82, v81, v1, s[16:17]
	s_waitcnt lgkmcnt(0)
	v_lshl_add_u64 v[92:93], s[14:15], 0, v[34:35]
	v_mov_b32_e32 v1, v0
	v_mov_b32_e32 v3, v2
	v_mov_b32_e32 v81, v80
	v_mov_b32_e32 v83, v82
	v_lshl_add_u64 v[86:87], v[92:93], 0, s[50:51]
	v_lshl_add_u64 v[88:89], v[92:93], 0, s[52:53]
	v_lshl_add_u64 v[90:91], v[92:93], 0, s[60:61]
	v_lshl_add_u64 v[92:93], v[92:93], 0, s[18:19]
	s_mov_b64 s[14:15], 0
	s_mov_b64 s[16:17], s[26:27]
	s_mov_b64 s[18:19], s[24:25]

.LBB0_2419:
	s_ashr_i32 s29, s28, 31
	s_lshl_b64 s[14:15], s[28:29], 12
	s_add_u32 s10, s26, s14
	s_addc_u32 s11, s27, s15
	s_add_u32 s12, s24, s14
	s_addc_u32 s13, s25, s15
	v_mov_b32_e32 v80, v32
	s_mov_b32 s0, 0
	v_mov_b32_e32 v76, 0
	v_mov_b32_e32 v77, v33
	v_mov_b32_e32 v78, 0
	v_mov_b32_e32 v79, v33
	v_mov_b32_e32 v56, 0
	v_mov_b32_e32 v57, v33
	v_mov_b32_e32 v52, 0
	v_mov_b32_e32 v53, v33
	v_mov_b32_e32 v50, 0
	v_mov_b32_e32 v51, v33
	v_mov_b32_e32 v46, 0
	v_mov_b32_e32 v47, v33
	v_mov_b32_e32 v30, 0
	v_mov_b32_e32 v31, v33
	v_mov_b32_e32 v26, 0
	v_mov_b32_e32 v27, v33
	v_mov_b32_e32 v24, 0
	v_mov_b32_e32 v25, v33
	v_mov_b32_e32 v20, 0
	v_mov_b32_e32 v21, v33
	v_mov_b32_e32 v18, 0
	v_mov_b32_e32 v19, v33
	v_mov_b32_e32 v14, 0
	v_mov_b32_e32 v15, v33
	v_mov_b32_e32 v10, 0
	v_mov_b32_e32 v11, v33
	v_mov_b32_e32 v8, 0
	v_mov_b32_e32 v9, v33
	v_mov_b32_e32 v4, 0
	v_mov_b32_e32 v5, v33
	v_mov_b32_e32 v0, 0
	v_mov_b32_e32 v1, v33
	v_mov_b32_e32 v64, 0
	v_mov_b32_e32 v65, v33
	v_mov_b32_e32 v68, 0
	v_mov_b32_e32 v69, v33
	v_mov_b32_e32 v2, 0
	v_mov_b32_e32 v3, v33
	v_mov_b32_e32 v6, 0
	v_mov_b32_e32 v7, v33
	v_mov_b32_e32 v12, 0
	v_mov_b32_e32 v13, v33
	v_mov_b32_e32 v16, 0
	v_mov_b32_e32 v17, v33
	v_mov_b32_e32 v22, 0
	v_mov_b32_e32 v23, v33
	v_mov_b32_e32 v28, 0
	v_mov_b32_e32 v29, v33
	v_mov_b32_e32 v44, 0
	v_mov_b32_e32 v45, v33
	v_mov_b32_e32 v48, 0
	v_mov_b32_e32 v49, v33
	v_mov_b32_e32 v54, 0
	v_mov_b32_e32 v55, v33
	v_mov_b32_e32 v58, 0
	v_mov_b32_e32 v59, v33
	v_mov_b32_e32 v60, 0
	v_mov_b32_e32 v61, v33
	v_mov_b32_e32 v62, 0
	v_mov_b32_e32 v63, v33
	v_mov_b32_e32 v66, 0
	v_mov_b32_e32 v67, v33
	v_mov_b32_e32 v70, 0
	v_mov_b32_e32 v71, v33
	v_mov_b32_e32 v72, 0
	v_mov_b32_e32 v73, v33
	v_mov_b32_e32 v74, 0
	v_mov_b32_e32 v75, v33
	v_lshl_add_u64 v[218:219], s[12:13], 0, v[34:35]
	global_load_dwordx2 v[202:203], v[218:219], off
	v_lshl_add_u64 v[218:219], s[10:11], 0, v[34:35]
	global_load_dwordx2 v[204:205], v[218:219], off
	v_lshl_add_u64 v[228:229], s[12:13], 0, v[34:35]
	v_add_co_u32_e32 v218, vcc, s39, v228
	s_nop 1
	v_addc_co_u32_e32 v219, vcc, 0, v229, vcc
	global_load_dwordx2 v[206:207], v[218:219], off offset:-4096
	v_lshl_add_u64 v[228:229], s[10:11], 0, v[34:35]
	v_add_co_u32_e32 v218, vcc, s39, v228
	s_nop 1
	v_addc_co_u32_e32 v219, vcc, 0, v229, vcc
	global_load_dwordx2 v[208:209], v[218:219], off offset:-4096
	v_lshl_add_u64 v[228:229], s[12:13], 0, v[34:35]
	v_add_co_u32_e32 v218, vcc, s39, v228
	s_nop 1
	v_addc_co_u32_e32 v219, vcc, 0, v229, vcc
	global_load_dwordx2 v[210:211], v[218:219], off
	v_lshl_add_u64 v[228:229], s[12:13], 0, v[34:35]
	v_add_co_u32_e32 v218, vcc, s41, v228
	s_nop 1
	v_addc_co_u32_e32 v219, vcc, 0, v229, vcc
	global_load_dwordx2 v[212:213], v[218:219], off
	v_lshl_add_u64 v[228:229], s[10:11], 0, v[34:35]
	v_add_co_u32_e32 v218, vcc, s39, v228
	s_nop 1
	v_addc_co_u32_e32 v219, vcc, 0, v229, vcc
	global_load_dwordx2 v[214:215], v[218:219], off
	v_lshl_add_u64 v[228:229], s[10:11], 0, v[34:35]
	v_add_co_u32_e32 v218, vcc, s41, v228
	s_nop 1
	v_addc_co_u32_e32 v219, vcc, 0, v229, vcc
	global_load_dwordx2 v[216:217], v[218:219], off
	v_ashrrev_i32_e32 v81, 31, v80
	v_lshlrev_b64 v[220:221], 4, v[80:81]
	v_lshl_add_u64 v[220:221], s[22:23], 0, v[220:221]
	global_load_dwordx4 v[220:223], v[220:221], off
	v_ashrrev_i32_e32 v81, 31, v80
	v_lshlrev_b64 v[228:229], 4, v[80:81]
	v_lshl_add_u64 v[224:225], s[20:21], 0, v[228:229]
	global_load_dwordx4 v[224:227], v[224:225], off
.LBB0_2420:
	s_nop 0
	s_nop 0
	v_add_u32_e32 v109, s0, v106
	s_nop 0
	v_add_u32_e32 v134, s0, v105
	v_add_u32_e32 v135, s0, v104
	v_add_u32_e32 v136, s0, v103
	ds_read_b128 v[82:85], v109
	ds_read_b128 v[86:89], v109 offset:32768
	ds_read_b128 v[90:93], v134
	ds_read_b128 v[94:97], v134 offset:32768
	ds_read_b128 v[110:113], v135
	ds_read_b128 v[114:117], v135 offset:32768
	ds_read_b128 v[118:121], v136
	ds_read_b128 v[122:125], v136 offset:32768
	v_add_u32_e32 v81, 0x10000, v109
	v_add_u32_e32 v137, 0x10000, v134
	v_add_u32_e32 v138, 0x10000, v135
	v_add_u32_e32 v139, 0x10000, v136
	v_add_u32_e32 v154, 0x18000, v135
	v_add_u32_e32 v158, 0x18000, v136
	v_add_u32_e32 v109, 0x18000, v109
	v_add_u32_e32 v145, 0x18000, v134
	ds_read_b128 v[126:129], v81
	ds_read_b128 v[130:133], v137
	ds_read_b128 v[134:137], v138
	ds_read_b128 v[138:141], v139
	ds_read_b128 v[146:149], v109
	ds_read_b128 v[150:153], v145
	ds_read_b128 v[154:157], v154
	ds_read_b128 v[158:161], v158
	s_nop 0
	s_addk_i32 s0, 0x1000
	s_add_u32 s10, s10, 0x200
	s_addc_u32 s11, s11, 0
	s_add_u32 s12, s12, 0x200
	s_addc_u32 s13, s13, 0
	v_add_u32_e32 v80, 64, v80
	s_cmpk_eq_u32 s0, 0x8000
	s_waitcnt vmcnt(0)
	v_mov_b64_e32 v[142:143], v[202:203]
	v_mov_b64_e32 v[170:171], v[204:205]
	v_mov_b64_e32 v[172:173], v[206:207]
	v_mov_b64_e32 v[174:175], v[208:209]
	v_mov_b64_e32 v[176:177], v[210:211]
	v_mov_b64_e32 v[178:179], v[212:213]
	v_mov_b64_e32 v[180:181], v[214:215]
	v_mov_b64_e32 v[182:183], v[216:217]
	v_mov_b64_e32 v[162:163], v[220:221]
	v_mov_b64_e32 v[164:165], v[222:223]
	v_mov_b64_e32 v[166:167], v[224:225]
	v_mov_b64_e32 v[168:169], v[226:227]
	s_cbranch_scc1 .Lswp_skip_1
	v_lshl_add_u64 v[218:219], s[12:13], 0, v[34:35]
	global_load_dwordx2 v[202:203], v[218:219], off
	v_lshl_add_u64 v[218:219], s[10:11], 0, v[34:35]
	global_load_dwordx2 v[204:205], v[218:219], off
	v_lshl_add_u64 v[228:229], s[12:13], 0, v[34:35]
	v_add_co_u32_e32 v218, vcc, s39, v228
	s_nop 1
	v_addc_co_u32_e32 v219, vcc, 0, v229, vcc
	global_load_dwordx2 v[206:207], v[218:219], off offset:-4096
	v_lshl_add_u64 v[228:229], s[10:11], 0, v[34:35]
	v_add_co_u32_e32 v218, vcc, s39, v228
	s_nop 1
	v_addc_co_u32_e32 v219, vcc, 0, v229, vcc
	global_load_dwordx2 v[208:209], v[218:219], off offset:-4096
	v_lshl_add_u64 v[228:229], s[12:13], 0, v[34:35]
	v_add_co_u32_e32 v218, vcc, s39, v228
	s_nop 1
	v_addc_co_u32_e32 v219, vcc, 0, v229, vcc
	global_load_dwordx2 v[210:211], v[218:219], off
	v_lshl_add_u64 v[228:229], s[12:13], 0, v[34:35]
	v_add_co_u32_e32 v218, vcc, s41, v228
	s_nop 1
	v_addc_co_u32_e32 v219, vcc, 0, v229, vcc
	global_load_dwordx2 v[212:213], v[218:219], off
	v_lshl_add_u64 v[228:229], s[10:11], 0, v[34:35]
	v_add_co_u32_e32 v218, vcc, s39, v228
	s_nop 1
	v_addc_co_u32_e32 v219, vcc, 0, v229, vcc
	global_load_dwordx2 v[214:215], v[218:219], off
	v_lshl_add_u64 v[228:229], s[10:11], 0, v[34:35]
	v_add_co_u32_e32 v218, vcc, s41, v228
	s_nop 1
	v_addc_co_u32_e32 v219, vcc, 0, v229, vcc
	global_load_dwordx2 v[216:217], v[218:219], off
	v_ashrrev_i32_e32 v81, 31, v80
	v_lshlrev_b64 v[220:221], 4, v[80:81]
	v_lshl_add_u64 v[220:221], s[22:23], 0, v[220:221]
	global_load_dwordx4 v[220:223], v[220:221], off
	v_ashrrev_i32_e32 v81, 31, v80
	v_lshlrev_b64 v[228:229], 4, v[80:81]
	v_lshl_add_u64 v[224:225], s[20:21], 0, v[228:229]
	global_load_dwordx4 v[224:227], v[224:225], off
.Lswp_skip_1:
	v_lshlrev_b32_e32 v99, 16, v142
	v_lshlrev_b32_e32 v185, 16, v170
	v_and_b32_e32 v187, 0xffff0000, v142
	v_and_b32_e32 v189, 0xffff0000, v170
	v_lshlrev_b32_e32 v191, 16, v143
	v_lshlrev_b32_e32 v193, 16, v171
	v_and_b32_e32 v143, 0xffff0000, v143
	v_and_b32_e32 v171, 0xffff0000, v171
	v_lshlrev_b32_e32 v98, 16, v172
	v_lshlrev_b32_e32 v184, 16, v174
	v_and_b32_e32 v186, 0xffff0000, v172
	v_and_b32_e32 v188, 0xffff0000, v174
	v_lshlrev_b32_e32 v190, 16, v173
	v_lshlrev_b32_e32 v192, 16, v175
	v_and_b32_e32 v142, 0xffff0000, v173
	v_and_b32_e32 v170, 0xffff0000, v175
	v_lshlrev_b32_e32 v173, 16, v176
	v_lshlrev_b32_e32 v172, 16, v178
	v_lshlrev_b32_e32 v175, 16, v180
	v_lshlrev_b32_e32 v174, 16, v182
	v_and_b32_e32 v195, 0xffff0000, v176
	v_and_b32_e32 v194, 0xffff0000, v178
	v_and_b32_e32 v197, 0xffff0000, v180
	v_and_b32_e32 v196, 0xffff0000, v182
	v_lshlrev_b32_e32 v199, 16, v177
	v_lshlrev_b32_e32 v198, 16, v179
	v_and_b32_e32 v177, 0xffff0000, v177
	v_and_b32_e32 v176, 0xffff0000, v179
	v_and_b32_e32 v179, 0xffff0000, v181
	v_and_b32_e32 v178, 0xffff0000, v183
	v_lshlrev_b32_e32 v201, 16, v181
	v_lshlrev_b32_e32 v200, 16, v183
	v_pk_add_f32 v[180:181], v[186:187], v[188:189]
	v_pk_add_f32 v[142:143], v[142:143], v[170:171]
	v_pk_add_f32 v[170:171], v[172:173], v[174:175]
	v_pk_add_f32 v[172:173], v[194:195], v[196:197]
	v_pk_add_f32 v[176:177], v[176:177], v[178:179]
	v_add_f32_e32 v81, 1.0, v162
	v_pk_add_f32 v[98:99], v[98:99], v[184:185]
	v_pk_add_f32 v[174:175], v[198:199], v[200:201]
	v_add_f32_e32 v109, 1.0, v163
	v_add_f32_e32 v145, 1.0, v164
	v_add_f32_e32 v186, 1.0, v165
	v_pk_mul_f32 v[162:163], v[180:181], v[180:181]
	v_pk_mul_f32 v[178:179], v[172:173], v[172:173]
	v_pk_mul_f32 v[184:185], v[176:177], v[176:177]
	v_mul_f32_e32 v81, v166, v81
	v_mul_f32_e32 v109, v167, v109
	v_mul_f32_e32 v145, v168, v145
	v_mul_f32_e32 v187, v169, v186
	v_pk_fma_f32 v[162:163], v[98:99], v[98:99], v[162:163]
	v_pk_fma_f32 v[166:167], v[170:171], v[170:171], v[178:179]
	v_pk_fma_f32 v[168:169], v[174:175], v[174:175], v[184:185]
	v_mul_f32_e32 v178, v81, v99
	v_mul_f32_e32 v98, v81, v98
	v_mul_f32_e32 v184, v81, v171
	v_mul_f32_e32 v170, v81, v170
	v_pk_add_f32 v[182:183], v[190:191], v[192:193]
	v_pk_mul_f32 v[164:165], v[142:143], v[142:143]
	v_mul_f32_e32 v186, v109, v181
	v_mul_f32_e32 v180, v109, v180
	v_mul_f32_e32 v188, v109, v173
	v_mul_f32_e32 v172, v109, v172
	s_waitcnt lgkmcnt(14)
	v_pk_fma_f32 v[74:75], v[178:179], v[82:83], v[74:75] op_sel_hi:[0,1,1]
	v_pk_fma_f32 v[72:73], v[178:179], v[84:85], v[72:73] op_sel_hi:[0,1,1]
	v_pk_fma_f32 v[48:49], v[98:99], v[82:83], v[48:49] op_sel_hi:[0,1,1]
	v_pk_fma_f32 v[44:45], v[98:99], v[84:85], v[44:45] op_sel_hi:[0,1,1]
	v_pk_fma_f32 v[68:69], v[82:83], v[184:185], v[68:69] op_sel_hi:[1,0,1]
	v_pk_fma_f32 v[64:65], v[84:85], v[184:185], v[64:65] op_sel_hi:[1,0,1]
	v_pk_fma_f32 v[24:25], v[82:83], v[170:171], v[24:25] op_sel_hi:[1,0,1]
	v_pk_fma_f32 v[20:21], v[84:85], v[170:171], v[20:21] op_sel_hi:[1,0,1]
	s_waitcnt lgkmcnt(13)
	v_pk_fma_f32 v[70:71], v[178:179], v[90:91], v[70:71] op_sel_hi:[0,1,1]
	v_pk_fma_f32 v[66:67], v[178:179], v[92:93], v[66:67] op_sel_hi:[0,1,1]
	v_pk_fma_f32 v[28:29], v[98:99], v[90:91], v[28:29] op_sel_hi:[0,1,1]
	v_pk_fma_f32 v[22:23], v[98:99], v[92:93], v[22:23] op_sel_hi:[0,1,1]
	v_pk_fma_f32 v[56:57], v[90:91], v[184:185], v[56:57] op_sel_hi:[1,0,1]
	v_pk_fma_f32 v[52:53], v[92:93], v[184:185], v[52:53] op_sel_hi:[1,0,1]
	v_pk_fma_f32 v[18:19], v[90:91], v[170:171], v[18:19] op_sel_hi:[1,0,1]
	v_pk_fma_f32 v[14:15], v[92:93], v[170:171], v[14:15] op_sel_hi:[1,0,1]
	s_waitcnt lgkmcnt(11)
	v_pk_fma_f32 v[62:63], v[178:179], v[110:111], v[62:63] op_sel_hi:[0,1,1]
	v_pk_fma_f32 v[60:61], v[178:179], v[112:113], v[60:61] op_sel_hi:[0,1,1]
	v_pk_fma_f32 v[16:17], v[98:99], v[110:111], v[16:17] op_sel_hi:[0,1,1]
	v_pk_fma_f32 v[12:13], v[98:99], v[112:113], v[12:13] op_sel_hi:[0,1,1]
	v_pk_fma_f32 v[50:51], v[184:185], v[110:111], v[50:51] op_sel_hi:[0,1,1]
	v_pk_fma_f32 v[46:47], v[184:185], v[112:113], v[46:47] op_sel_hi:[0,1,1]
	v_pk_fma_f32 v[10:11], v[110:111], v[170:171], v[10:11] op_sel_hi:[1,0,1]
	v_pk_fma_f32 v[8:9], v[112:113], v[170:171], v[8:9] op_sel_hi:[1,0,1]
	s_waitcnt lgkmcnt(9)
	v_pk_fma_f32 v[58:59], v[178:179], v[118:119], v[58:59] op_sel_hi:[0,1,1]
	v_pk_fma_f32 v[54:55], v[178:179], v[120:121], v[54:55] op_sel_hi:[0,1,1]
	v_pk_fma_f32 v[6:7], v[98:99], v[118:119], v[6:7] op_sel_hi:[0,1,1]
	v_pk_fma_f32 v[2:3], v[98:99], v[120:121], v[2:3] op_sel_hi:[0,1,1]
	v_pk_fma_f32 v[30:31], v[184:185], v[118:119], v[30:31] op_sel_hi:[0,1,1]
	v_pk_fma_f32 v[26:27], v[184:185], v[120:121], v[26:27] op_sel_hi:[0,1,1]
	v_pk_fma_f32 v[4:5], v[118:119], v[170:171], v[4:5] op_sel_hi:[1,0,1]
	v_pk_fma_f32 v[0:1], v[120:121], v[170:171], v[0:1] op_sel_hi:[1,0,1]
	v_pk_fma_f32 v[164:165], v[182:183], v[182:183], v[164:165]
	v_mul_f32_e32 v190, v145, v183
	v_mul_f32_e32 v182, v145, v182
	v_mul_f32_e32 v192, v145, v175
	v_mul_f32_e32 v174, v145, v174
	v_pk_fma_f32 v[74:75], v[186:187], v[86:87], v[74:75] op_sel_hi:[0,1,1]
	v_pk_fma_f32 v[72:73], v[186:187], v[88:89], v[72:73] op_sel_hi:[0,1,1]
	v_pk_fma_f32 v[48:49], v[180:181], v[86:87], v[48:49] op_sel_hi:[0,1,1]
	v_pk_fma_f32 v[44:45], v[180:181], v[88:89], v[44:45] op_sel_hi:[0,1,1]
	v_pk_fma_f32 v[68:69], v[188:189], v[86:87], v[68:69] op_sel_hi:[0,1,1]
	v_pk_fma_f32 v[64:65], v[188:189], v[88:89], v[64:65] op_sel_hi:[0,1,1]
	v_pk_fma_f32 v[24:25], v[172:173], v[86:87], v[24:25] op_sel_hi:[0,1,1]
	v_pk_fma_f32 v[20:21], v[172:173], v[88:89], v[20:21] op_sel_hi:[0,1,1]
	v_pk_fma_f32 v[70:71], v[186:187], v[94:95], v[70:71] op_sel_hi:[0,1,1]
	v_pk_fma_f32 v[66:67], v[186:187], v[96:97], v[66:67] op_sel_hi:[0,1,1]
	v_pk_fma_f32 v[28:29], v[180:181], v[94:95], v[28:29] op_sel_hi:[0,1,1]
	v_pk_fma_f32 v[22:23], v[180:181], v[96:97], v[22:23] op_sel_hi:[0,1,1]
	v_pk_fma_f32 v[56:57], v[188:189], v[94:95], v[56:57] op_sel_hi:[0,1,1]
	v_pk_fma_f32 v[52:53], v[188:189], v[96:97], v[52:53] op_sel_hi:[0,1,1]
	v_pk_fma_f32 v[18:19], v[172:173], v[94:95], v[18:19] op_sel_hi:[0,1,1]
	v_pk_fma_f32 v[14:15], v[172:173], v[96:97], v[14:15] op_sel_hi:[0,1,1]
	v_pk_fma_f32 v[62:63], v[186:187], v[114:115], v[62:63] op_sel_hi:[0,1,1]
	v_pk_fma_f32 v[60:61], v[186:187], v[116:117], v[60:61] op_sel_hi:[0,1,1]
	v_pk_fma_f32 v[16:17], v[180:181], v[114:115], v[16:17] op_sel_hi:[0,1,1]
	v_pk_fma_f32 v[12:13], v[180:181], v[116:117], v[12:13] op_sel_hi:[0,1,1]
	v_pk_fma_f32 v[50:51], v[188:189], v[114:115], v[50:51] op_sel_hi:[0,1,1]
	v_pk_fma_f32 v[46:47], v[188:189], v[116:117], v[46:47] op_sel_hi:[0,1,1]
	v_pk_fma_f32 v[10:11], v[172:173], v[114:115], v[10:11] op_sel_hi:[0,1,1]
	v_pk_fma_f32 v[8:9], v[172:173], v[116:117], v[8:9] op_sel_hi:[0,1,1]
	s_waitcnt lgkmcnt(8)
	v_pk_fma_f32 v[58:59], v[186:187], v[122:123], v[58:59] op_sel_hi:[0,1,1]
	v_pk_fma_f32 v[54:55], v[186:187], v[124:125], v[54:55] op_sel_hi:[0,1,1]
	v_pk_fma_f32 v[6:7], v[180:181], v[122:123], v[6:7] op_sel_hi:[0,1,1]
	v_pk_fma_f32 v[2:3], v[180:181], v[124:125], v[2:3] op_sel_hi:[0,1,1]
	v_pk_fma_f32 v[30:31], v[188:189], v[122:123], v[30:31] op_sel_hi:[0,1,1]
	v_pk_fma_f32 v[26:27], v[188:189], v[124:125], v[26:27] op_sel_hi:[0,1,1]
	v_pk_fma_f32 v[4:5], v[172:173], v[122:123], v[4:5] op_sel_hi:[0,1,1]
	v_pk_fma_f32 v[0:1], v[172:173], v[124:125], v[0:1] op_sel_hi:[0,1,1]
	v_mul_f32_e32 v194, v187, v143
	v_mul_f32_e32 v142, v187, v142
	v_mul_f32_e32 v196, v187, v177
	v_mul_f32_e32 v176, v187, v176
	v_pk_add_f32 v[162:163], v[162:163], v[164:165]
	v_pk_add_f32 v[164:165], v[166:167], v[168:169]
	s_waitcnt lgkmcnt(7)
	v_pk_fma_f32 v[74:75], v[190:191], v[126:127], v[74:75] op_sel_hi:[0,1,1]
	v_pk_fma_f32 v[72:73], v[190:191], v[128:129], v[72:73] op_sel_hi:[0,1,1]
	v_pk_fma_f32 v[48:49], v[182:183], v[126:127], v[48:49] op_sel_hi:[0,1,1]
	v_pk_fma_f32 v[44:45], v[182:183], v[128:129], v[44:45] op_sel_hi:[0,1,1]
	v_pk_fma_f32 v[68:69], v[192:193], v[126:127], v[68:69] op_sel_hi:[0,1,1]
	v_pk_fma_f32 v[64:65], v[192:193], v[128:129], v[64:65] op_sel_hi:[0,1,1]
	v_pk_fma_f32 v[24:25], v[174:175], v[126:127], v[24:25] op_sel_hi:[0,1,1]
	v_pk_fma_f32 v[20:21], v[174:175], v[128:129], v[20:21] op_sel_hi:[0,1,1]
	s_waitcnt lgkmcnt(6)
	v_pk_fma_f32 v[70:71], v[190:191], v[130:131], v[70:71] op_sel_hi:[0,1,1]
	v_pk_fma_f32 v[66:67], v[190:191], v[132:133], v[66:67] op_sel_hi:[0,1,1]
	v_pk_fma_f32 v[28:29], v[182:183], v[130:131], v[28:29] op_sel_hi:[0,1,1]
	v_pk_fma_f32 v[22:23], v[182:183], v[132:133], v[22:23] op_sel_hi:[0,1,1]
	v_pk_fma_f32 v[56:57], v[192:193], v[130:131], v[56:57] op_sel_hi:[0,1,1]
	v_pk_fma_f32 v[52:53], v[192:193], v[132:133], v[52:53] op_sel_hi:[0,1,1]
	v_pk_fma_f32 v[18:19], v[174:175], v[130:131], v[18:19] op_sel_hi:[0,1,1]
	v_pk_fma_f32 v[14:15], v[174:175], v[132:133], v[14:15] op_sel_hi:[0,1,1]
	s_waitcnt lgkmcnt(5)
	v_pk_fma_f32 v[62:63], v[190:191], v[134:135], v[62:63] op_sel_hi:[0,1,1]
	v_pk_fma_f32 v[60:61], v[190:191], v[136:137], v[60:61] op_sel_hi:[0,1,1]
	v_pk_fma_f32 v[16:17], v[182:183], v[134:135], v[16:17] op_sel_hi:[0,1,1]
	v_pk_fma_f32 v[12:13], v[182:183], v[136:137], v[12:13] op_sel_hi:[0,1,1]
	v_pk_fma_f32 v[50:51], v[192:193], v[134:135], v[50:51] op_sel_hi:[0,1,1]
	v_pk_fma_f32 v[46:47], v[192:193], v[136:137], v[46:47] op_sel_hi:[0,1,1]
	v_pk_fma_f32 v[10:11], v[174:175], v[134:135], v[10:11] op_sel_hi:[0,1,1]
	v_pk_fma_f32 v[8:9], v[174:175], v[136:137], v[8:9] op_sel_hi:[0,1,1]
	s_waitcnt lgkmcnt(4)
	v_pk_fma_f32 v[58:59], v[190:191], v[138:139], v[58:59] op_sel_hi:[0,1,1]
	v_pk_fma_f32 v[54:55], v[190:191], v[140:141], v[54:55] op_sel_hi:[0,1,1]
	v_pk_fma_f32 v[6:7], v[182:183], v[138:139], v[6:7] op_sel_hi:[0,1,1]
	v_pk_fma_f32 v[2:3], v[182:183], v[140:141], v[2:3] op_sel_hi:[0,1,1]
	v_pk_fma_f32 v[30:31], v[192:193], v[138:139], v[30:31] op_sel_hi:[0,1,1]
	v_pk_fma_f32 v[26:27], v[192:193], v[140:141], v[26:27] op_sel_hi:[0,1,1]
	v_pk_fma_f32 v[4:5], v[174:175], v[138:139], v[4:5] op_sel_hi:[0,1,1]
	v_pk_fma_f32 v[0:1], v[174:175], v[140:141], v[0:1] op_sel_hi:[0,1,1]
	v_pk_add_f32 v[78:79], v[78:79], v[162:163]
	v_pk_add_f32 v[76:77], v[76:77], v[164:165]
	s_waitcnt lgkmcnt(3)
	v_pk_fma_f32 v[74:75], v[194:195], v[146:147], v[74:75] op_sel_hi:[0,1,1]
	v_pk_fma_f32 v[72:73], v[194:195], v[148:149], v[72:73] op_sel_hi:[0,1,1]
	v_pk_fma_f32 v[48:49], v[142:143], v[146:147], v[48:49] op_sel_hi:[0,1,1]
	v_pk_fma_f32 v[44:45], v[142:143], v[148:149], v[44:45] op_sel_hi:[0,1,1]
	v_pk_fma_f32 v[68:69], v[196:197], v[146:147], v[68:69] op_sel_hi:[0,1,1]
	v_pk_fma_f32 v[64:65], v[196:197], v[148:149], v[64:65] op_sel_hi:[0,1,1]
	v_pk_fma_f32 v[24:25], v[176:177], v[146:147], v[24:25] op_sel_hi:[0,1,1]
	v_pk_fma_f32 v[20:21], v[176:177], v[148:149], v[20:21] op_sel_hi:[0,1,1]
	s_waitcnt lgkmcnt(2)
	v_pk_fma_f32 v[70:71], v[194:195], v[150:151], v[70:71] op_sel_hi:[0,1,1]
	v_pk_fma_f32 v[66:67], v[194:195], v[152:153], v[66:67] op_sel_hi:[0,1,1]
	v_pk_fma_f32 v[28:29], v[142:143], v[150:151], v[28:29] op_sel_hi:[0,1,1]
	v_pk_fma_f32 v[22:23], v[142:143], v[152:153], v[22:23] op_sel_hi:[0,1,1]
	v_pk_fma_f32 v[56:57], v[196:197], v[150:151], v[56:57] op_sel_hi:[0,1,1]
	v_pk_fma_f32 v[52:53], v[196:197], v[152:153], v[52:53] op_sel_hi:[0,1,1]
	v_pk_fma_f32 v[18:19], v[176:177], v[150:151], v[18:19] op_sel_hi:[0,1,1]
	v_pk_fma_f32 v[14:15], v[176:177], v[152:153], v[14:15] op_sel_hi:[0,1,1]
	s_waitcnt lgkmcnt(1)
	v_pk_fma_f32 v[62:63], v[194:195], v[154:155], v[62:63] op_sel_hi:[0,1,1]
	v_pk_fma_f32 v[60:61], v[194:195], v[156:157], v[60:61] op_sel_hi:[0,1,1]
	v_pk_fma_f32 v[16:17], v[142:143], v[154:155], v[16:17] op_sel_hi:[0,1,1]
	v_pk_fma_f32 v[12:13], v[142:143], v[156:157], v[12:13] op_sel_hi:[0,1,1]
	v_pk_fma_f32 v[50:51], v[196:197], v[154:155], v[50:51] op_sel_hi:[0,1,1]
	v_pk_fma_f32 v[46:47], v[196:197], v[156:157], v[46:47] op_sel_hi:[0,1,1]
	v_pk_fma_f32 v[10:11], v[176:177], v[154:155], v[10:11] op_sel_hi:[0,1,1]
	v_pk_fma_f32 v[8:9], v[176:177], v[156:157], v[8:9] op_sel_hi:[0,1,1]
	s_waitcnt lgkmcnt(0)
	v_pk_fma_f32 v[58:59], v[194:195], v[158:159], v[58:59] op_sel_hi:[0,1,1]
	v_pk_fma_f32 v[54:55], v[194:195], v[160:161], v[54:55] op_sel_hi:[0,1,1]
	v_pk_fma_f32 v[6:7], v[142:143], v[158:159], v[6:7] op_sel_hi:[0,1,1]
	v_pk_fma_f32 v[2:3], v[142:143], v[160:161], v[2:3] op_sel_hi:[0,1,1]
	v_pk_fma_f32 v[30:31], v[196:197], v[158:159], v[30:31] op_sel_hi:[0,1,1]
	v_pk_fma_f32 v[26:27], v[196:197], v[160:161], v[26:27] op_sel_hi:[0,1,1]
	v_pk_fma_f32 v[4:5], v[176:177], v[158:159], v[4:5] op_sel_hi:[0,1,1]
	v_pk_fma_f32 v[0:1], v[176:177], v[160:161], v[0:1] op_sel_hi:[0,1,1]
	s_cbranch_scc0 .LBB0_2420
	v_mov_b32_e32 v80, v144
	s_ashr_i32 s31, s30, 31
	v_lshlrev_b32_e32 v82, 2, v80
	v_xor_b32_e32 v80, 4, v82
	ds_bpermute_b32 v81, v80, v79
	v_mov_b32_e32 v80, v144
	v_xor_b32_e32 v84, 8, v82
	v_lshlrev_b32_e32 v83, 2, v80
	v_xor_b32_e32 v80, 4, v83
	ds_bpermute_b32 v80, v80, v78
	v_xor_b32_e32 v85, 8, v83
	v_xor_b32_e32 v86, 16, v82
	v_xor_b32_e32 v87, 16, v83
	v_xor_b32_e32 v88, 32, v82
	s_waitcnt lgkmcnt(0)
	v_pk_add_f32 v[78:79], v[78:79], v[80:81]
	ds_bpermute_b32 v81, v84, v79
	ds_bpermute_b32 v80, v85, v78
	v_xor_b32_e32 v89, 32, v83
	s_ashr_i32 s35, s34, 31
	s_ashr_i32 s37, s36, 31
	s_lshl_b64 s[16:17], s[30:31], 12
	s_waitcnt lgkmcnt(0)
	v_pk_add_f32 v[78:79], v[78:79], v[80:81]
	ds_bpermute_b32 v81, v86, v79
	ds_bpermute_b32 v80, v87, v78
	s_lshl_b64 s[44:45], s[34:35], 12
	s_lshl_b64 s[46:47], s[36:37], 12
	v_lshl_add_u64 v[84:85], v[36:37], 0, s[14:15]
	v_lshl_add_u64 v[86:87], v[38:39], 0, s[14:15]
	s_waitcnt lgkmcnt(0)
	v_pk_add_f32 v[78:79], v[78:79], v[80:81]
	ds_bpermute_b32 v81, v88, v79
	ds_bpermute_b32 v80, v89, v78
	v_xor_b32_e32 v88, 64, v82
	v_xor_b32_e32 v89, 64, v83
	v_xor_b32_e32 v82, 0x80, v82
	v_xor_b32_e32 v83, 0x80, v83
	s_waitcnt lgkmcnt(0)
	v_pk_add_f32 v[78:79], v[78:79], v[80:81]
	ds_bpermute_b32 v81, v88, v79
	ds_bpermute_b32 v80, v89, v78
	v_mov_b64_e32 v[96:97], v[42:43]
	v_mov_b64_e32 v[98:99], v[40:41]
	s_waitcnt lgkmcnt(0)
	v_pk_add_f32 v[78:79], v[78:79], v[80:81]
	ds_bpermute_b32 v81, v82, v79
	v_mov_b32_e32 v82, v144
	ds_bpermute_b32 v80, v83, v78
	v_lshlrev_b32_e32 v88, 2, v82
	v_xor_b32_e32 v82, 4, v88
	ds_bpermute_b32 v83, v82, v77
	v_mov_b32_e32 v82, v144
	v_xor_b32_e32 v90, 8, v88
	v_lshlrev_b32_e32 v89, 2, v82
	v_xor_b32_e32 v82, 4, v89
	ds_bpermute_b32 v82, v82, v76
	v_xor_b32_e32 v91, 8, v89
	v_xor_b32_e32 v92, 16, v89
	s_waitcnt lgkmcnt(2)
	v_pk_add_f32 v[78:79], v[78:79], v[80:81]
	v_mov_b64_e32 v[80:81], s[40:41]
	s_waitcnt lgkmcnt(0)
	v_pk_add_f32 v[76:77], v[76:77], v[82:83]
	ds_bpermute_b32 v83, v90, v77
	ds_bpermute_b32 v82, v91, v76
	v_xor_b32_e32 v91, 16, v88
	v_pk_fma_f32 v[78:79], v[78:79], s[38:39], v[80:81] op_sel_hi:[1,0,0]
	s_waitcnt lgkmcnt(0)
	v_pk_add_f32 v[76:77], v[76:77], v[82:83]
	ds_bpermute_b32 v83, v91, v77
	ds_bpermute_b32 v82, v92, v76
	v_mul_f32_e32 v90, 0x4b800000, v79
	v_cmp_gt_f32_e32 vcc, s51, v79
	v_xor_b32_e32 v91, 32, v89
	v_xor_b32_e32 v92, 64, v89
	v_cndmask_b32_e32 v79, v79, v90, vcc
	v_xor_b32_e32 v90, 32, v88
	s_waitcnt lgkmcnt(0)
	v_pk_add_f32 v[76:77], v[76:77], v[82:83]
	ds_bpermute_b32 v83, v90, v77
	ds_bpermute_b32 v82, v91, v76
	v_xor_b32_e32 v91, 64, v88
	v_rsq_f32_e32 v90, v79
	v_mul_f32_e32 v79, 0x4b800000, v78
	v_cmp_gt_f32_e64 s[10:11], s51, v78
	s_waitcnt lgkmcnt(0)
	v_pk_add_f32 v[76:77], v[76:77], v[82:83]
	ds_bpermute_b32 v83, v91, v77
	ds_bpermute_b32 v82, v92, v76
	v_cndmask_b32_e64 v78, v78, v79, s[10:11]
	v_rsq_f32_e32 v91, v78
	v_xor_b32_e32 v88, 0x80, v88
	v_xor_b32_e32 v89, 0x80, v89
	s_waitcnt lgkmcnt(0)
	v_pk_add_f32 v[78:79], v[76:77], v[82:83]
	ds_bpermute_b32 v83, v88, v79
	ds_bpermute_b32 v82, v89, v78
	v_mul_f32_e32 v76, 0x45800000, v90
	v_cndmask_b32_e32 v76, v90, v76, vcc
	v_mul_f32_e32 v77, 0x45800000, v91
	s_waitcnt lgkmcnt(0)
	v_pk_add_f32 v[78:79], v[78:79], v[82:83]
	s_nop 0
	v_pk_fma_f32 v[78:79], v[78:79], s[38:39], v[80:81] op_sel_hi:[1,0,0]
	s_nop 0
	v_mul_f32_e32 v80, 0x4b800000, v79
	v_cmp_gt_f32_e32 vcc, s51, v79
	v_cmp_gt_f32_e64 s[12:13], s51, v78
	s_nop 0
	v_cndmask_b32_e32 v79, v79, v80, vcc
	v_mul_f32_e32 v80, 0x4b800000, v78
	v_rsq_f32_e32 v79, v79
	v_cndmask_b32_e64 v78, v78, v80, s[12:13]
	v_rsq_f32_e32 v81, v78
	v_cndmask_b32_e64 v78, v91, v77, s[10:11]
	s_load_dwordx2 s[10:11], s[18:19], 0x118
	v_mul_f32_e32 v77, 0x45800000, v79
	v_cndmask_b32_e32 v80, v79, v77, vcc
	v_mul_f32_e32 v77, 0x45800000, v81
	v_cndmask_b32_e64 v82, v81, v77, s[12:13]
	s_waitcnt lgkmcnt(0)
	v_lshl_add_u64 v[94:95], s[10:11], 0, v[34:35]
	v_mov_b32_e32 v77, v76
	v_mov_b32_e32 v79, v78
	v_mov_b32_e32 v81, v80
	v_mov_b32_e32 v83, v82
	v_lshl_add_u64 v[88:89], v[94:95], 0, s[16:17]
	v_lshl_add_u64 v[90:91], v[94:95], 0, s[44:45]
	v_lshl_add_u64 v[92:93], v[94:95], 0, s[46:47]
	v_lshl_add_u64 v[94:95], v[94:95], 0, s[14:15]
	s_mov_b64 s[10:11], 0
